# v049 with plain (not nt) stores for the bf16 MoE weights written by the prologue conversion
# baseline (speedup 1.0000x reference)
; #define LAS __attribute__((address_space(3)))
; __device__ __forceinline__ void cvt_item(const float* W, int K, int N, bf16_t* WT, int drow0, int k0, int n0, LAS float* scr, int lane) {
;     f32x4 v[16];
;     const int lr = lane >> 4, lc4 = (lane & 15) * 4;
; #pragma unroll
;     for (int i = 0; i < 16; ++i) v[i] = __builtin_nontemporal_load((const f32x4*)(W + (size_t)(k0 + 4 * i + lr) * N + n0 + lc4));
; #pragma unroll
;     for (int i = 0; i < 16; ++i) { LAS float* d = scr + (4 * i + lr) * 65 + lc4; d[0] = v[i][0]; d[1] = v[i][1]; d[2] = v[i][2]; d[3] = v[i][3]; }
; __device__ __forceinline__ void phase_cvt_moe(LAS unsigned char* lds, const CvtMoe a) {
;     ...
;         if (r < 2 * IG) { const int up = r / IG; r %= IG; const int nblk = FF / 64, kb = r / nblk, nb = r % nblk, n0 = nb * 64;
;             cvt_item((up ? a.wu : a.wg) + (size_t)e * D * FF, D, FF, a.gu + (size_t)e * 2 * FF * D, (n0 / 128) * 256 + up * 128 + (n0 % 128), kb * 64, n0, scr, lane); }
;         else { r -= 2 * IG; const int nblk = D / 64, kb = r / nblk, nb = r % nblk; cvt_item(a.wd + (size_t)e * FF * D, FF, D, a.dn + (size_t)e * D * FF, nb * 64, kb * 64, nb * 64, scr, lane); }
.LBB0_58:
	v_mul_hi_i32 v51, v5, s3
	v_lshrrev_b32_e32 v52, 31, v51
	v_ashrrev_i32_e32 v51, 9, v51
	v_add_u32_e32 v51, v51, v52
	v_mul_i32_i24_e32 v53, 0x840, v51
	v_sub_u32_e32 v52, v5, v53
	v_cmp_lt_i32_e32 vcc, s10, v52
	s_and_saveexec_b64 s[8:9], vcc
	s_xor_b64 s[8:9], exec, s[8:9]
	s_cbranch_execz .LBB0_60
	v_lshlrev_b32_e32 v52, 6, v53
	v_sub_u32_e32 v118, v18, v52
	v_lshlrev_b32_e32 v52, 2, v53
	v_sub_u32_e32 v52, v16, v52
	v_and_b32_e32 v52, 0x7fffffc0, v52
	v_mov_b64_e32 v[54:55], s[84:85]
	v_and_b32_e32 v119, 0x3c0, v118
	v_add_u32_e32 v120, 0xffffea00, v52
	v_mad_i64_i32 v[54:55], s[30:31], v51, s11, v[54:55]
	v_or_b32_e32 v112, v120, v6
	v_lshlrev_b32_e32 v52, 2, v119
	v_mov_b32_e32 v53, v3
	v_lshl_add_u64 v[52:53], v[54:55], 0, v[52:53]
	v_mov_b32_e32 v113, v3
	v_or_b32_e32 v54, 4, v112
	v_mov_b32_e32 v55, v3
	v_or_b32_e32 v60, 8, v112
	v_mov_b32_e32 v61, v3
	v_or_b32_e32 v62, 12, v112
	v_mov_b32_e32 v63, v3
	v_or_b32_e32 v68, 16, v112
	v_mov_b32_e32 v69, v3
	v_or_b32_e32 v70, 20, v112
	v_mov_b32_e32 v71, v3
	v_or_b32_e32 v76, 24, v112
	v_mov_b32_e32 v77, v3
	v_or_b32_e32 v78, 28, v112
	v_mov_b32_e32 v79, v3
	v_or_b32_e32 v84, 32, v112
	v_mov_b32_e32 v85, v3
	v_or_b32_e32 v86, 36, v112
	v_mov_b32_e32 v87, v3
	v_or_b32_e32 v92, 40, v112
	v_mov_b32_e32 v93, v3
	v_or_b32_e32 v94, 44, v112
	v_mov_b32_e32 v95, v3
	v_or_b32_e32 v100, 48, v112
	v_mov_b32_e32 v101, v3
	v_or_b32_e32 v102, 52, v112
	v_mov_b32_e32 v103, v3
	v_or_b32_e32 v108, 56, v112
	v_mov_b32_e32 v109, v3
	v_lshl_add_u64 v[114:115], v[52:53], 0, v[2:3]
	v_lshlrev_b64 v[52:53], 12, v[112:113]
	v_lshlrev_b64 v[54:55], 12, v[54:55]
	v_lshlrev_b64 v[60:61], 12, v[60:61]
	v_lshlrev_b64 v[62:63], 12, v[62:63]
	v_lshlrev_b64 v[68:69], 12, v[68:69]
	v_lshlrev_b64 v[70:71], 12, v[70:71]
	v_lshlrev_b64 v[76:77], 12, v[76:77]
	v_lshlrev_b64 v[78:79], 12, v[78:79]
	v_lshlrev_b64 v[84:85], 12, v[84:85]
	v_lshlrev_b64 v[86:87], 12, v[86:87]
	v_lshlrev_b64 v[92:93], 12, v[92:93]
	v_lshlrev_b64 v[94:95], 12, v[94:95]
	v_lshlrev_b64 v[100:101], 12, v[100:101]
	v_lshlrev_b64 v[102:103], 12, v[102:103]
	v_lshlrev_b64 v[108:109], 12, v[108:109]
	v_lshl_add_u64 v[52:53], v[114:115], 0, v[52:53]
	v_lshl_add_u64 v[56:57], v[114:115], 0, v[54:55]
	v_lshl_add_u64 v[60:61], v[114:115], 0, v[60:61]
	v_lshl_add_u64 v[64:65], v[114:115], 0, v[62:63]
	v_lshl_add_u64 v[68:69], v[114:115], 0, v[68:69]
	v_lshl_add_u64 v[72:73], v[114:115], 0, v[70:71]
	v_lshl_add_u64 v[76:77], v[114:115], 0, v[76:77]
	v_lshl_add_u64 v[80:81], v[114:115], 0, v[78:79]
	v_lshl_add_u64 v[84:85], v[114:115], 0, v[84:85]
	v_lshl_add_u64 v[88:89], v[114:115], 0, v[86:87]
	v_lshl_add_u64 v[92:93], v[114:115], 0, v[92:93]
	v_lshl_add_u64 v[96:97], v[114:115], 0, v[94:95]
	v_lshl_add_u64 v[100:101], v[114:115], 0, v[100:101]
	v_lshl_add_u64 v[104:105], v[114:115], 0, v[102:103]
	v_lshl_add_u64 v[108:109], v[114:115], 0, v[108:109]
	v_or_b32_e32 v112, 60, v112
	global_load_dwordx4 v[52:55], v[52:53], off nt
	s_nop 0
	global_load_dwordx4 v[56:59], v[56:57], off nt
	s_nop 0
	global_load_dwordx4 v[60:63], v[60:61], off nt
	s_nop 0
	global_load_dwordx4 v[64:67], v[64:65], off nt
	s_nop 0
	global_load_dwordx4 v[68:71], v[68:69], off nt
	s_nop 0
	global_load_dwordx4 v[72:75], v[72:73], off nt
	s_nop 0
	global_load_dwordx4 v[76:79], v[76:77], off nt
	s_nop 0
	global_load_dwordx4 v[80:83], v[80:81], off nt
	s_nop 0
	global_load_dwordx4 v[84:87], v[84:85], off nt
	s_nop 0
	global_load_dwordx4 v[88:91], v[88:89], off nt
	s_nop 0
	global_load_dwordx4 v[92:95], v[92:93], off nt
	s_nop 0
	global_load_dwordx4 v[96:99], v[96:97], off nt
	s_nop 0
	global_load_dwordx4 v[100:103], v[100:101], off nt
	s_nop 0
	global_load_dwordx4 v[104:107], v[104:105], off nt
	v_lshlrev_b64 v[112:113], 12, v[112:113]
	global_load_dwordx4 v[108:111], v[108:109], off nt
	v_lshl_add_u64 v[112:113], v[114:115], 0, v[112:113]
	global_load_dwordx4 v[112:115], v[112:113], off nt
	v_mul_hi_i32_i24_e32 v117, 0x580000, v51
	v_mul_i32_i24_e32 v116, 0x580000, v51
	v_add_u32_e32 v51, 0x38e0, v20
	s_waitcnt vmcnt(15)
	ds_write2_b32 v20, v52, v53 offset1:1
	ds_write2_b32 v20, v54, v55 offset0:2 offset1:3
	s_waitcnt vmcnt(14)
	ds_write2_b32 v21, v56, v57 offset1:1
	ds_write2_b32 v22, v58, v59 offset1:1
	s_waitcnt vmcnt(13)
	ds_write2_b32 v23, v60, v61 offset1:1
	ds_write2_b32 v24, v62, v63 offset1:1
	s_waitcnt vmcnt(12)
	ds_write2_b32 v25, v64, v65 offset1:1
	ds_write2_b32 v26, v66, v67 offset1:1
	s_waitcnt vmcnt(11)
	ds_write2_b32 v27, v68, v69 offset1:1
	ds_write2_b32 v28, v70, v71 offset1:1
	s_waitcnt vmcnt(10)
	ds_write2_b32 v29, v72, v73 offset1:1
	ds_write2_b32 v30, v74, v75 offset1:1
	s_waitcnt vmcnt(9)
	ds_write2_b32 v31, v76, v77 offset1:1
	ds_write2_b32 v32, v78, v79 offset1:1
	s_waitcnt vmcnt(8)
	ds_write2_b32 v33, v80, v81 offset1:1
	ds_write2_b32 v34, v82, v83 offset1:1
	s_waitcnt vmcnt(7)
	ds_write2_b32 v35, v84, v85 offset1:1
	ds_write2_b32 v36, v86, v87 offset1:1
	s_waitcnt vmcnt(6)
	ds_write2_b32 v37, v88, v89 offset1:1
	ds_write2_b32 v38, v90, v91 offset1:1
	s_waitcnt vmcnt(5)
	ds_write2_b32 v39, v92, v93 offset1:1
	ds_write2_b32 v40, v94, v95 offset1:1
	s_waitcnt vmcnt(4)
	ds_write2_b32 v41, v96, v97 offset1:1
	ds_write2_b32 v42, v98, v99 offset1:1
	s_waitcnt vmcnt(3)
	ds_write2_b32 v43, v100, v101 offset1:1
	ds_write2_b32 v44, v102, v103 offset1:1
	s_waitcnt vmcnt(2)
	ds_write2_b32 v45, v104, v105 offset1:1
	ds_write2_b32 v46, v106, v107 offset1:1
	v_readlane_b32 s30, v250, 8
	s_waitcnt vmcnt(1)
	ds_write2_b32 v51, v108, v109 offset1:1
	v_add_u32_e32 v51, 0x38e8, v20
	ds_write2_b32 v51, v110, v111 offset1:1
	v_add_u32_e32 v51, 0x3cf0, v20
	s_waitcnt vmcnt(0)
; #define LAS __attribute__((address_space(3)))
; __device__ __forceinline__ unsigned cvt_pk_bf16(float lo, float hi) { const f32x2 v = {lo, hi}; const bf16v2_t r = __builtin_convertvector(v, bf16v2_t); return __builtin_bit_cast(unsigned, r); }
; __device__ __forceinline__ void cvt_item(const float* W, int K, int N, bf16_t* WT, int drow0, int k0, int n0, LAS float* scr, int lane) {
;     ...
;     for (int i = 0; i < 16; ++i) { LAS float* d = scr + (4 * i + lr) * 65 + lc4; d[0] = v[i][0]; d[1] = v[i][1]; d[2] = v[i][2]; d[3] = v[i][3]; }
;     asm volatile("s_waitcnt lgkmcnt(0)" ::: "memory");
;     const int c = lane & 7;
; #pragma unroll
;     for (int j = 0; j < 8; ++j) { const int n = (lane >> 3) + 8 * j; const LAS float* s = scr + (8 * c) * 65 + n;
;         u32x4 o; o.x = cvt_pk_bf16(s[0 * 65], s[1 * 65]); o.y = cvt_pk_bf16(s[2 * 65], s[3 * 65]); o.z = cvt_pk_bf16(s[4 * 65], s[5 * 65]); o.w = cvt_pk_bf16(s[6 * 65], s[7 * 65]);
;         __builtin_nontemporal_store(o, (u32x4*)(WT + ((size_t)((drow0 + n) >> 7) * (K >> 6) + (k0 >> 6)) * 8192 + ((drow0 + n) & 127) * 64 + 8 * c)); }
;     asm volatile("s_waitcnt lgkmcnt(0)" ::: "memory");
	ds_write2_b32 v51, v112, v113 offset1:1
	v_add_u32_e32 v51, 0x3cf8, v20
	ds_write2_b32 v51, v114, v115 offset1:1
	s_waitcnt lgkmcnt(0)
	ds_read2_b32 v[56:57], v8 offset0:65 offset1:73
	ds_read2_b32 v[58:59], v8 offset1:8
	ds_read2_b32 v[60:61], v8 offset0:130 offset1:138
	ds_read2_b32 v[62:63], v8 offset0:195 offset1:203
	v_add_u32_e32 v51, 0x400, v8
	ds_read2_b32 v[64:65], v51 offset0:4 offset1:12
	ds_read2_b32 v[66:67], v51 offset0:69 offset1:77
	ds_read2_b32 v[68:69], v51 offset0:134 offset1:142
	ds_read2_b32 v[70:71], v51 offset0:199 offset1:207
	v_lshrrev_b32_e32 v72, 6, v120
	s_waitcnt lgkmcnt(6)
	v_cvt_pk_bf16_f32 v52, v58, v56
	v_bfe_u32 v58, v118, 7, 3
	v_readlane_b32 s31, v250, 9
	v_or_b32_e32 v56, v119, v7
	v_mad_u32_u24 v72, v58, 44, v72
	v_mov_b32_e32 v73, v3
	v_lshl_add_u64 v[116:117], s[30:31], 0, v[116:117]
	v_lshlrev_b64 v[72:73], 14, v[72:73]
	v_lshlrev_b32_e32 v56, 7, v56
	v_lshl_add_u64 v[72:73], v[116:117], 0, v[72:73]
	v_and_b32_e32 v74, 0x2380, v56
	v_mov_b32_e32 v75, v3
	v_lshl_add_u64 v[74:75], v[72:73], 0, v[74:75]
	v_lshlrev_b32_e32 v76, 1, v4
	v_mov_b32_e32 v77, v3
	v_or_b32_e32 v56, v119, v9
	s_waitcnt lgkmcnt(4)
	v_cvt_pk_bf16_f32 v53, v60, v62
	s_waitcnt lgkmcnt(2)
	v_cvt_pk_bf16_f32 v54, v64, v66
	s_waitcnt lgkmcnt(0)
	v_cvt_pk_bf16_f32 v55, v68, v70
	v_lshl_add_u64 v[74:75], v[74:75], 0, v[76:77]
	v_lshlrev_b32_e32 v56, 7, v56
	global_store_dwordx4 v[74:75], v[52:55], off
	v_and_b32_e32 v56, 0x2780, v56
	s_nop 0
	v_cvt_pk_bf16_f32 v52, v59, v57
	v_mov_b32_e32 v57, v3
	v_lshl_add_u64 v[56:57], v[72:73], 0, v[56:57]
	v_cvt_pk_bf16_f32 v53, v61, v63
	v_cvt_pk_bf16_f32 v54, v65, v67
	v_cvt_pk_bf16_f32 v55, v69, v71
	v_lshl_add_u64 v[56:57], v[56:57], 0, v[76:77]
	ds_read2_b32 v[58:59], v8 offset0:16 offset1:24
	ds_read2_b32 v[60:61], v8 offset0:81 offset1:89
	ds_read2_b32 v[62:63], v8 offset0:146 offset1:154
	ds_read2_b32 v[64:65], v8 offset0:211 offset1:219
	ds_read2_b32 v[66:67], v51 offset0:20 offset1:28
	ds_read2_b32 v[68:69], v51 offset0:85 offset1:93
	ds_read2_b32 v[70:71], v51 offset0:150 offset1:158
	ds_read2_b32 v[74:75], v51 offset0:215 offset1:223
	global_store_dwordx4 v[56:57], v[52:55], off
	v_or_b32_e32 v56, v119, v10
	v_lshlrev_b32_e32 v56, 7, v56
	v_and_b32_e32 v56, 0x2b80, v56
	v_mov_b32_e32 v57, v3
	v_lshl_add_u64 v[56:57], v[72:73], 0, v[56:57]
	s_waitcnt lgkmcnt(6)
	v_cvt_pk_bf16_f32 v52, v58, v60
	s_waitcnt lgkmcnt(4)
	v_cvt_pk_bf16_f32 v53, v62, v64
	s_waitcnt lgkmcnt(2)
	v_cvt_pk_bf16_f32 v54, v66, v68
	s_waitcnt lgkmcnt(0)
	v_cvt_pk_bf16_f32 v55, v70, v74
	v_lshl_add_u64 v[56:57], v[56:57], 0, v[76:77]
	global_store_dwordx4 v[56:57], v[52:55], off
	v_or_b32_e32 v56, v119, v11
	v_lshlrev_b32_e32 v56, 7, v56
	v_and_b32_e32 v56, 0x2f80, v56
	v_mov_b32_e32 v57, v3
	v_lshl_add_u64 v[56:57], v[72:73], 0, v[56:57]
	v_cvt_pk_bf16_f32 v52, v59, v61
	v_cvt_pk_bf16_f32 v53, v63, v65
	v_cvt_pk_bf16_f32 v54, v67, v69
	v_cvt_pk_bf16_f32 v55, v71, v75
	v_lshl_add_u64 v[56:57], v[56:57], 0, v[76:77]
	ds_read2_b32 v[58:59], v8 offset0:32 offset1:40
	ds_read2_b32 v[60:61], v8 offset0:97 offset1:105
	ds_read2_b32 v[62:63], v8 offset0:162 offset1:170
	ds_read2_b32 v[64:65], v8 offset0:227 offset1:235
	ds_read2_b32 v[66:67], v51 offset0:36 offset1:44
	ds_read2_b32 v[68:69], v51 offset0:101 offset1:109
	ds_read2_b32 v[70:71], v51 offset0:166 offset1:174
	ds_read2_b32 v[74:75], v51 offset0:231 offset1:239
	global_store_dwordx4 v[56:57], v[52:55], off
	v_or_b32_e32 v56, v119, v12
	v_lshlrev_b32_e32 v56, 7, v56
	v_and_b32_e32 v56, 0x3380, v56
	v_mov_b32_e32 v57, v3
	v_lshl_add_u64 v[56:57], v[72:73], 0, v[56:57]
	s_waitcnt lgkmcnt(6)
	v_cvt_pk_bf16_f32 v52, v58, v60
	s_waitcnt lgkmcnt(4)
	v_cvt_pk_bf16_f32 v53, v62, v64
	s_waitcnt lgkmcnt(2)
	v_cvt_pk_bf16_f32 v54, v66, v68
	s_waitcnt lgkmcnt(0)
	v_cvt_pk_bf16_f32 v55, v70, v74
	v_lshl_add_u64 v[56:57], v[56:57], 0, v[76:77]
	global_store_dwordx4 v[56:57], v[52:55], off
	v_or_b32_e32 v56, v119, v13
	v_lshlrev_b32_e32 v56, 7, v56
	v_cvt_pk_bf16_f32 v52, v59, v61
	v_cvt_pk_bf16_f32 v53, v63, v65
	v_cvt_pk_bf16_f32 v54, v67, v69
	v_cvt_pk_bf16_f32 v55, v71, v75
	v_and_b32_e32 v56, 0x3780, v56
	v_mov_b32_e32 v57, v3
	ds_read2_b32 v[58:59], v8 offset0:48 offset1:56
	ds_read2_b32 v[60:61], v8 offset0:113 offset1:121
	ds_read2_b32 v[62:63], v8 offset0:178 offset1:186
	ds_read2_b32 v[64:65], v8 offset0:243 offset1:251
	ds_read2_b32 v[66:67], v51 offset0:52 offset1:60
	ds_read2_b32 v[68:69], v51 offset0:117 offset1:125
	ds_read2_b32 v[70:71], v51 offset0:182 offset1:190
	ds_read2_b32 v[74:75], v51 offset0:247 offset1:255
	v_lshl_add_u64 v[56:57], v[72:73], 0, v[56:57]
	v_or_b32_e32 v51, v119, v14
	v_lshl_add_u64 v[56:57], v[56:57], 0, v[76:77]
	v_lshlrev_b32_e32 v51, 7, v51
	global_store_dwordx4 v[56:57], v[52:55], off
	v_and_b32_e32 v56, 0x3b80, v51
	v_mov_b32_e32 v57, v3
	v_lshl_add_u64 v[56:57], v[72:73], 0, v[56:57]
	v_or_b32_e32 v51, v119, v15
	s_waitcnt lgkmcnt(6)
	v_cvt_pk_bf16_f32 v52, v58, v60
	s_waitcnt lgkmcnt(4)
	v_cvt_pk_bf16_f32 v53, v62, v64
	s_waitcnt lgkmcnt(2)
	v_cvt_pk_bf16_f32 v54, v66, v68
	s_waitcnt lgkmcnt(0)
	v_cvt_pk_bf16_f32 v55, v70, v74
	v_lshl_add_u64 v[56:57], v[56:57], 0, v[76:77]
	v_lshlrev_b32_e32 v51, 7, v51
	global_store_dwordx4 v[56:57], v[52:55], off
	v_and_b32_e32 v56, 0x3f80, v51
	v_mov_b32_e32 v57, v3
	v_lshl_add_u64 v[56:57], v[72:73], 0, v[56:57]
	v_cvt_pk_bf16_f32 v52, v59, v61
	v_cvt_pk_bf16_f32 v53, v63, v65
	v_cvt_pk_bf16_f32 v54, v67, v69
	v_cvt_pk_bf16_f32 v55, v71, v75
	v_lshl_add_u64 v[56:57], v[56:57], 0, v[76:77]
	global_store_dwordx4 v[56:57], v[52:55], off
	s_waitcnt lgkmcnt(0)
; #define LAS __attribute__((address_space(3)))
; __device__ __forceinline__ void cvt_item(const float* W, int K, int N, bf16_t* WT, int drow0, int k0, int n0, LAS float* scr, int lane) {
;     ...
; #pragma unroll
;     for (int i = 0; i < 16; ++i) v[i] = __builtin_nontemporal_load((const f32x4*)(W + (size_t)(k0 + 4 * i + lr) * N + n0 + lc4));
; #pragma unroll
;     for (int i = 0; i < 16; ++i) { LAS float* d = scr + (4 * i + lr) * 65 + lc4; d[0] = v[i][0]; d[1] = v[i][1]; d[2] = v[i][2]; d[3] = v[i][3]; }
; __device__ __forceinline__ void phase_cvt_moe(LAS unsigned char* lds, const CvtMoe a) {
;     ...
;     for (int it = gw; it < 2 * NE * (2 * IG + ID); it += NGW) {
;         const int e = it / (2 * IG + ID); int r = it % (2 * IG + ID);
;         if (r < 2 * IG) { const int up = r / IG; r %= IG; const int nblk = FF / 64, kb = r / nblk, nb = r % nblk, n0 = nb * 64;
;             cvt_item((up ? a.wu : a.wg) + (size_t)e * D * FF, D, FF, a.gu + (size_t)e * 2 * FF * D, (n0 / 128) * 256 + up * 128 + (n0 % 128), kb * 64, n0, scr, lane); }
.LBB0_60:
	s_andn2_saveexec_b64 s[8:9], s[8:9]
	s_cbranch_execz .LBB0_57
	v_mul_i32_i24_e32 v53, 0xba3, v52
	v_lshrrev_b32_e32 v54, 31, v53
	v_ashrrev_i32_e32 v53, 21, v53
	v_add_u16_e32 v117, v53, v54
	v_mul_lo_u16_e32 v53, 0x2c0, v117
	v_sub_u16_e32 v53, v52, v53
	v_mul_i32_i24_sdwa v54, sext(v53), s12 dst_sel:DWORD dst_unused:UNUSED_PAD src0_sel:WORD_0 src1_sel:DWORD
	v_lshrrev_b32_e32 v55, 31, v54
	v_ashrrev_i32_e32 v54, 17, v54
	v_add_u16_e32 v54, v54, v55
	v_bfe_i32 v116, v54, 0, 16
	v_mul_lo_u16_e32 v54, 44, v54
	v_add_u32_e32 v52, 0x2bf, v52
	v_sub_u16_e32 v122, v53, v54
	v_mov_b32_e32 v53, s83
	v_mov_b32_e32 v54, s81
	v_cmp_gt_u32_e32 vcc, s10, v52
	v_mov_b32_e32 v52, s82
	v_lshlrev_b32_sdwa v118, v47, sext(v122) dst_sel:DWORD dst_unused:UNUSED_PAD src0_sel:DWORD src1_sel:WORD_0
	v_cndmask_b32_e32 v53, v53, v54, vcc
	v_mov_b32_e32 v54, s80
	v_cndmask_b32_e32 v52, v52, v54, vcc
	v_mad_i64_i32 v[52:53], s[30:31], v51, s11, v[52:53]
	v_lshl_or_b32 v54, v116, 6, v6
	v_ashrrev_i32_e32 v119, 31, v118
	v_lshl_add_u64 v[52:53], v[118:119], 2, v[52:53]
	v_mul_i32_i24_e32 v54, 0xb00, v54
	v_lshl_add_u64 v[52:53], v[52:53], 0, v[2:3]
	v_ashrrev_i32_e32 v55, 31, v54
	v_lshl_add_u64 v[112:113], v[54:55], 2, v[52:53]
	v_add_co_u32_e32 v56, vcc, s13, v112
	v_readlane_b32 s30, v250, 6
	s_nop 0
	v_addc_co_u32_e32 v57, vcc, 0, v113, vcc
	v_add_co_u32_e32 v60, vcc, s14, v112
	global_load_dwordx4 v[52:55], v[112:113], off nt
	s_nop 0
	global_load_dwordx4 v[56:59], v[56:57], off nt
	v_addc_co_u32_e32 v61, vcc, 0, v113, vcc
	v_add_co_u32_e32 v64, vcc, s15, v112
	v_readlane_b32 s31, v250, 7
	s_nop 0
	v_addc_co_u32_e32 v65, vcc, 0, v113, vcc
	v_add_co_u32_e32 v68, vcc, s16, v112
	global_load_dwordx4 v[60:63], v[60:61], off nt
	s_nop 0
	global_load_dwordx4 v[64:67], v[64:65], off nt
	v_addc_co_u32_e32 v69, vcc, 0, v113, vcc
	v_add_co_u32_e32 v72, vcc, s17, v112
	v_mov_b64_e32 v[120:121], s[30:31]
	s_nop 0
	v_addc_co_u32_e32 v73, vcc, 0, v113, vcc
	v_add_co_u32_e32 v76, vcc, s18, v112
	global_load_dwordx4 v[68:71], v[68:69], off nt
	s_nop 0
	global_load_dwordx4 v[72:75], v[72:73], off nt
	v_addc_co_u32_e32 v77, vcc, 0, v113, vcc
	v_add_co_u32_e32 v80, vcc, s19, v112
	v_ashrrev_i16_e32 v119, 15, v118
	s_nop 0
	v_addc_co_u32_e32 v81, vcc, 0, v113, vcc
	v_add_co_u32_e32 v84, vcc, s20, v112
	global_load_dwordx4 v[76:79], v[76:77], off nt
	s_nop 0
	global_load_dwordx4 v[80:83], v[80:81], off nt
	v_addc_co_u32_e32 v85, vcc, 0, v113, vcc
	v_add_co_u32_e32 v88, vcc, s21, v112
	v_mad_i64_i32 v[120:121], s[30:31], v51, s11, v[120:121]
	s_nop 0
	v_addc_co_u32_e32 v89, vcc, 0, v113, vcc
	v_add_co_u32_e32 v92, vcc, s22, v112
	global_load_dwordx4 v[84:87], v[84:85], off nt
	s_nop 0
	global_load_dwordx4 v[88:91], v[88:89], off nt
	v_addc_co_u32_e32 v93, vcc, 0, v113, vcc
	v_add_co_u32_e32 v96, vcc, s23, v112
	v_lshrrev_b16_e32 v51, 7, v122
	s_nop 0
	v_addc_co_u32_e32 v97, vcc, 0, v113, vcc
	v_add_co_u32_e32 v100, vcc, s24, v112
	global_load_dwordx4 v[92:95], v[92:93], off nt
	s_nop 0
	global_load_dwordx4 v[96:99], v[96:97], off nt
	v_addc_co_u32_e32 v101, vcc, 0, v113, vcc
	v_add_co_u32_e32 v104, vcc, s25, v112
	v_lshrrev_b16_e32 v119, 9, v119
	s_nop 0
	v_addc_co_u32_e32 v105, vcc, 0, v113, vcc
	v_add_co_u32_e32 v108, vcc, s26, v112
	global_load_dwordx4 v[100:103], v[100:101], off nt
	s_nop 0
	global_load_dwordx4 v[104:107], v[104:105], off nt
	v_addc_co_u32_e32 v109, vcc, 0, v113, vcc
	global_load_dwordx4 v[108:111], v[108:109], off nt
	v_add_co_u32_e32 v112, vcc, s27, v112
	v_and_b32_e32 v51, 1, v51
	s_nop 0
	v_addc_co_u32_e32 v113, vcc, 0, v113, vcc
	global_load_dwordx4 v[112:115], v[112:113], off nt
	v_add_u16_e32 v119, v118, v119
	v_add_u16_e32 v51, v122, v51
	v_and_b32_e32 v119, 0xffffff80, v119
	v_ashrrev_i16_sdwa v51, v48, sext(v51) dst_sel:DWORD dst_unused:UNUSED_PAD src0_sel:DWORD src1_sel:BYTE_0
	v_sub_u16_e32 v118, v118, v119
	v_lshlrev_b32_sdwa v51, v49, sext(v51) dst_sel:DWORD dst_unused:UNUSED_PAD src0_sel:DWORD src1_sel:WORD_0
	v_lshlrev_b32_sdwa v117, v50, sext(v117) dst_sel:DWORD dst_unused:UNUSED_PAD src0_sel:DWORD src1_sel:WORD_0
	v_bfe_i32 v118, v118, 0, 16
	v_add3_u32 v51, v51, v117, v118
	v_ashrrev_i32_e32 v117, 31, v116
	s_waitcnt vmcnt(15)
	ds_write2_b32 v20, v52, v53 offset1:1
	ds_write2_b32 v20, v54, v55 offset0:2 offset1:3
	s_waitcnt vmcnt(14)
	ds_write2_b32 v21, v56, v57 offset1:1
	ds_write2_b32 v22, v58, v59 offset1:1
	s_waitcnt vmcnt(13)
	ds_write2_b32 v23, v60, v61 offset1:1
	ds_write2_b32 v24, v62, v63 offset1:1
	s_waitcnt vmcnt(12)
	ds_write2_b32 v25, v64, v65 offset1:1
	ds_write2_b32 v26, v66, v67 offset1:1
	s_waitcnt vmcnt(11)
	ds_write2_b32 v27, v68, v69 offset1:1
	ds_write2_b32 v28, v70, v71 offset1:1
	s_waitcnt vmcnt(10)
	ds_write2_b32 v29, v72, v73 offset1:1
	ds_write2_b32 v30, v74, v75 offset1:1
	s_waitcnt vmcnt(9)
	ds_write2_b32 v31, v76, v77 offset1:1
	ds_write2_b32 v32, v78, v79 offset1:1
	s_waitcnt vmcnt(8)
	ds_write2_b32 v33, v80, v81 offset1:1
	ds_write2_b32 v34, v82, v83 offset1:1
	s_waitcnt vmcnt(7)
	ds_write2_b32 v35, v84, v85 offset1:1
	ds_write2_b32 v36, v86, v87 offset1:1
	s_waitcnt vmcnt(6)
	ds_write2_b32 v37, v88, v89 offset1:1
	ds_write2_b32 v38, v90, v91 offset1:1
	s_waitcnt vmcnt(5)
	ds_write2_b32 v39, v92, v93 offset1:1
	ds_write2_b32 v40, v94, v95 offset1:1
	s_waitcnt vmcnt(4)
	ds_write2_b32 v41, v96, v97 offset1:1
	ds_write2_b32 v42, v98, v99 offset1:1
	s_waitcnt vmcnt(3)
	ds_write2_b32 v43, v100, v101 offset1:1
	ds_write2_b32 v44, v102, v103 offset1:1
	s_waitcnt vmcnt(2)
	ds_write2_b32 v45, v104, v105 offset1:1
	ds_write2_b32 v46, v106, v107 offset1:1
	v_add_u32_e32 v52, 0x38e0, v20
	v_add_u32_e32 v78, 0x400, v8
	s_waitcnt vmcnt(1)
; #define LAS __attribute__((address_space(3)))
; __device__ __forceinline__ unsigned cvt_pk_bf16(float lo, float hi) { const f32x2 v = {lo, hi}; const bf16v2_t r = __builtin_convertvector(v, bf16v2_t); return __builtin_bit_cast(unsigned, r); }
; __device__ __forceinline__ void cvt_item(const float* W, int K, int N, bf16_t* WT, int drow0, int k0, int n0, LAS float* scr, int lane) {
;     ...
;     for (int i = 0; i < 16; ++i) { LAS float* d = scr + (4 * i + lr) * 65 + lc4; d[0] = v[i][0]; d[1] = v[i][1]; d[2] = v[i][2]; d[3] = v[i][3]; }
;     asm volatile("s_waitcnt lgkmcnt(0)" ::: "memory");
;     const int c = lane & 7;
; #pragma unroll
;     for (int j = 0; j < 8; ++j) { const int n = (lane >> 3) + 8 * j; const LAS float* s = scr + (8 * c) * 65 + n;
;         u32x4 o; o.x = cvt_pk_bf16(s[0 * 65], s[1 * 65]); o.y = cvt_pk_bf16(s[2 * 65], s[3 * 65]); o.z = cvt_pk_bf16(s[4 * 65], s[5 * 65]); o.w = cvt_pk_bf16(s[6 * 65], s[7 * 65]);
;         __builtin_nontemporal_store(o, (u32x4*)(WT + ((size_t)((drow0 + n) >> 7) * (K >> 6) + (k0 >> 6)) * 8192 + ((drow0 + n) & 127) * 64 + 8 * c)); }
;     asm volatile("s_waitcnt lgkmcnt(0)" ::: "memory");
	ds_write2_b32 v52, v108, v109 offset1:1
	v_add_u32_e32 v52, 0x38e8, v20
	ds_write2_b32 v52, v110, v111 offset1:1
	v_add_u32_e32 v52, 0x3cf0, v20
	v_ashrrev_i32_e32 v72, 7, v51
	v_ashrrev_i32_e32 v73, 31, v72
	s_waitcnt vmcnt(0)
	ds_write2_b32 v52, v112, v113 offset1:1
	v_add_u32_e32 v52, 0x3cf8, v20
	ds_write2_b32 v52, v114, v115 offset1:1
	s_waitcnt lgkmcnt(0)
	ds_read2_b32 v[56:57], v8 offset0:65 offset1:73
	ds_read2_b32 v[58:59], v8 offset1:8
	ds_read2_b32 v[60:61], v8 offset0:130 offset1:138
	ds_read2_b32 v[62:63], v8 offset0:195 offset1:203
	ds_read2_b32 v[64:65], v78 offset0:4 offset1:12
	ds_read2_b32 v[66:67], v78 offset0:69 offset1:77
	ds_read2_b32 v[68:69], v78 offset0:134 offset1:142
	ds_read2_b32 v[70:71], v78 offset0:199 offset1:207
	v_lshlrev_b64 v[72:73], 18, v[72:73]
	s_waitcnt lgkmcnt(6)
	v_cvt_pk_bf16_f32 v52, v58, v56
	v_or_b32_e32 v56, v51, v7
	v_lshlrev_b64 v[74:75], 14, v[116:117]
	v_lshl_add_u64 v[72:73], v[120:121], 0, v[72:73]
	v_lshlrev_b32_e32 v56, 7, v56
	v_lshl_add_u64 v[72:73], v[72:73], 0, v[74:75]
	v_and_b32_e32 v74, 0x3f80, v56
	v_mov_b32_e32 v75, v3
	v_lshl_add_u64 v[74:75], v[72:73], 0, v[74:75]
	v_lshlrev_b32_e32 v76, 1, v4
	v_mov_b32_e32 v77, v3
	v_or_b32_e32 v56, v51, v9
	s_waitcnt lgkmcnt(4)
	v_cvt_pk_bf16_f32 v53, v60, v62
	s_waitcnt lgkmcnt(2)
	v_cvt_pk_bf16_f32 v54, v64, v66
	s_waitcnt lgkmcnt(0)
	v_cvt_pk_bf16_f32 v55, v68, v70
	v_lshl_add_u64 v[74:75], v[74:75], 0, v[76:77]
	v_lshlrev_b32_e32 v56, 7, v56
	global_store_dwordx4 v[74:75], v[52:55], off
	v_and_b32_e32 v56, 0x3f80, v56
	s_nop 0
	v_cvt_pk_bf16_f32 v52, v59, v57
	v_mov_b32_e32 v57, v3
	v_lshl_add_u64 v[56:57], v[72:73], 0, v[56:57]
	v_cvt_pk_bf16_f32 v53, v61, v63
	v_cvt_pk_bf16_f32 v54, v65, v67
	v_cvt_pk_bf16_f32 v55, v69, v71
	v_lshl_add_u64 v[56:57], v[56:57], 0, v[76:77]
	ds_read2_b32 v[58:59], v8 offset0:16 offset1:24
	ds_read2_b32 v[60:61], v8 offset0:81 offset1:89
	ds_read2_b32 v[62:63], v8 offset0:146 offset1:154
	ds_read2_b32 v[64:65], v8 offset0:211 offset1:219
	ds_read2_b32 v[66:67], v78 offset0:20 offset1:28
	ds_read2_b32 v[68:69], v78 offset0:85 offset1:93
	ds_read2_b32 v[70:71], v78 offset0:150 offset1:158
	ds_read2_b32 v[74:75], v78 offset0:215 offset1:223
	global_store_dwordx4 v[56:57], v[52:55], off
	v_or_b32_e32 v56, v51, v10
	v_lshlrev_b32_e32 v56, 7, v56
	v_and_b32_e32 v56, 0x3f80, v56
	v_mov_b32_e32 v57, v3
	v_lshl_add_u64 v[56:57], v[72:73], 0, v[56:57]
	s_waitcnt lgkmcnt(6)
	v_cvt_pk_bf16_f32 v52, v58, v60
	s_waitcnt lgkmcnt(4)
	v_cvt_pk_bf16_f32 v53, v62, v64
	s_waitcnt lgkmcnt(2)
	v_cvt_pk_bf16_f32 v54, v66, v68
	s_waitcnt lgkmcnt(0)
	v_cvt_pk_bf16_f32 v55, v70, v74
	v_lshl_add_u64 v[56:57], v[56:57], 0, v[76:77]
	global_store_dwordx4 v[56:57], v[52:55], off
	v_or_b32_e32 v56, v51, v11
	v_lshlrev_b32_e32 v56, 7, v56
	v_and_b32_e32 v56, 0x3f80, v56
	v_mov_b32_e32 v57, v3
	v_lshl_add_u64 v[56:57], v[72:73], 0, v[56:57]
	v_cvt_pk_bf16_f32 v52, v59, v61
	v_cvt_pk_bf16_f32 v53, v63, v65
	v_cvt_pk_bf16_f32 v54, v67, v69
	v_cvt_pk_bf16_f32 v55, v71, v75
	v_lshl_add_u64 v[56:57], v[56:57], 0, v[76:77]
	ds_read2_b32 v[58:59], v8 offset0:32 offset1:40
	ds_read2_b32 v[60:61], v8 offset0:97 offset1:105
	ds_read2_b32 v[62:63], v8 offset0:162 offset1:170
	ds_read2_b32 v[64:65], v8 offset0:227 offset1:235
	ds_read2_b32 v[66:67], v78 offset0:36 offset1:44
	ds_read2_b32 v[68:69], v78 offset0:101 offset1:109
	ds_read2_b32 v[70:71], v78 offset0:166 offset1:174
	ds_read2_b32 v[74:75], v78 offset0:231 offset1:239
	global_store_dwordx4 v[56:57], v[52:55], off
	v_or_b32_e32 v56, v51, v12
	v_lshlrev_b32_e32 v56, 7, v56
	v_and_b32_e32 v56, 0x3f80, v56
	v_mov_b32_e32 v57, v3
	v_lshl_add_u64 v[56:57], v[72:73], 0, v[56:57]
	s_waitcnt lgkmcnt(6)
	v_cvt_pk_bf16_f32 v52, v58, v60
	s_waitcnt lgkmcnt(4)
	v_cvt_pk_bf16_f32 v53, v62, v64
	s_waitcnt lgkmcnt(2)
	v_cvt_pk_bf16_f32 v54, v66, v68
	s_waitcnt lgkmcnt(0)
	v_cvt_pk_bf16_f32 v55, v70, v74
	v_lshl_add_u64 v[56:57], v[56:57], 0, v[76:77]
	global_store_dwordx4 v[56:57], v[52:55], off
	v_or_b32_e32 v56, v51, v13
	v_lshlrev_b32_e32 v56, 7, v56
	v_and_b32_e32 v56, 0x3f80, v56
	v_mov_b32_e32 v57, v3
	v_lshl_add_u64 v[56:57], v[72:73], 0, v[56:57]
	v_cvt_pk_bf16_f32 v52, v59, v61
	v_cvt_pk_bf16_f32 v53, v63, v65
	v_cvt_pk_bf16_f32 v54, v67, v69
	v_cvt_pk_bf16_f32 v55, v71, v75
	v_lshl_add_u64 v[56:57], v[56:57], 0, v[76:77]
	ds_read2_b32 v[58:59], v8 offset0:48 offset1:56
	ds_read2_b32 v[60:61], v8 offset0:113 offset1:121
	ds_read2_b32 v[62:63], v8 offset0:178 offset1:186
	ds_read2_b32 v[64:65], v8 offset0:243 offset1:251
	ds_read2_b32 v[66:67], v78 offset0:52 offset1:60
	ds_read2_b32 v[68:69], v78 offset0:117 offset1:125
	ds_read2_b32 v[70:71], v78 offset0:182 offset1:190
	ds_read2_b32 v[74:75], v78 offset0:247 offset1:255
	global_store_dwordx4 v[56:57], v[52:55], off
	v_or_b32_e32 v56, v51, v14
	v_lshlrev_b32_e32 v56, 7, v56
	v_and_b32_e32 v56, 0x3f80, v56
	v_mov_b32_e32 v57, v3
	v_lshl_add_u64 v[56:57], v[72:73], 0, v[56:57]
	v_or_b32_e32 v51, v51, v15
	s_waitcnt lgkmcnt(6)
	v_cvt_pk_bf16_f32 v52, v58, v60
	s_waitcnt lgkmcnt(4)
	v_cvt_pk_bf16_f32 v53, v62, v64
	s_waitcnt lgkmcnt(2)
	v_cvt_pk_bf16_f32 v54, v66, v68
	s_waitcnt lgkmcnt(0)
	v_cvt_pk_bf16_f32 v55, v70, v74
	v_lshl_add_u64 v[56:57], v[56:57], 0, v[76:77]
	v_lshlrev_b32_e32 v51, 7, v51
	global_store_dwordx4 v[56:57], v[52:55], off
	v_and_b32_e32 v56, 0x3f80, v51
	v_mov_b32_e32 v57, v3
	v_lshl_add_u64 v[56:57], v[72:73], 0, v[56:57]
	v_cvt_pk_bf16_f32 v52, v59, v61
	v_cvt_pk_bf16_f32 v53, v63, v65
	v_cvt_pk_bf16_f32 v54, v67, v69
	v_cvt_pk_bf16_f32 v55, v71, v75
	v_lshl_add_u64 v[56:57], v[56:57], 0, v[76:77]
	global_store_dwordx4 v[56:57], v[52:55], off
	s_waitcnt lgkmcnt(0)
	s_branch .LBB0_57
